# attention (first call site): block-gate mean-k loads batched per past block (16 loads up front, counted vmcnt) instead of 56 serialized vmcnt(0) round trips
# baseline (speedup 1.0000x reference)
.LBB0_2645:
	v_readfirstlane_b32 s80, v0
	s_lshr_b32 s25, s80, 6
	s_lshl_b32 s2, s25, 13
	s_add_i32 s77, s2, 0
	s_add_i32 s77, s77, 0x10840
	v_add_u32_e32 v191, s77, v201
	ds_write_b128 v205, v[4:7]
	ds_write_b128 v206, v[8:11]
	v_add_u32_e32 v2, s24, v202
	v_mov_b64_e32 v[4:5], s[90:91]
	v_add_u32_e32 v16, s24, v203
	v_mov_b64_e32 v[12:13], s[70:71]
	v_mad_u64_u32 v[6:7], s[2:3], v2, s33, v[4:5]
	v_mov_b32_e32 v189, v3
	v_mad_u64_u32 v[4:5], s[2:3], v16, s33, v[4:5]
	v_mad_u64_u32 v[14:15], s[2:3], v2, s33, v[12:13]
	v_lshl_add_u64 v[6:7], v[6:7], 0, v[188:189]
	v_lshl_add_u64 v[8:9], v[4:5], 0, v[188:189]
	v_lshl_add_u64 v[14:15], v[14:15], 0, v[188:189]
	v_mad_u64_u32 v[12:13], s[2:3], v16, s33, v[12:13]
	global_load_dwordx4 v[4:7], v[6:7], off
	s_nop 0
	global_load_dwordx4 v[8:11], v[8:9], off
	v_lshl_add_u64 v[16:17], v[12:13], 0, v[188:189]
	global_load_dwordx4 v[12:15], v[14:15], off
	s_nop 0
	global_load_dwordx4 v[52:55], v[16:17], off
	s_waitcnt vmcnt(4)
	ds_read_b128 v[174:177], v191
	ds_read_b128 v[170:173], v191 offset:1024
	ds_read_b128 v[166:169], v191 offset:2048
	ds_read_b128 v[162:165], v191 offset:3072
	s_lshr_b32 s76, s24, 8
	s_cmpk_lt_u32 s24, 0x100
	v_mov_b32_e32 v217, 0
	s_cbranch_scc1 .LBB0_2656
	s_cmpk_gt_u32 s24, 0x3ff
	s_mov_b64 s[10:11], -1
	s_cbranch_scc0 .LBB0_2654
	v_lshlrev_b32_e32 v2, 2, v184
	global_load_dwordx4 v[110:113], v2, s[8:9] offset:16
	global_load_dwordx4 v[106:109], v2, s[8:9]
	global_load_dwordx4 v[118:121], v2, s[8:9] offset:80
	global_load_dwordx4 v[114:117], v2, s[8:9] offset:64
	global_load_dwordx4 v[126:129], v2, s[8:9] offset:144
	global_load_dwordx4 v[122:125], v2, s[8:9] offset:128
	global_load_dwordx4 v[134:137], v2, s[8:9] offset:208
	global_load_dwordx4 v[130:133], v2, s[8:9] offset:192
	global_load_dwordx4 v[142:145], v2, s[8:9] offset:272
	global_load_dwordx4 v[138:141], v2, s[8:9] offset:256
	global_load_dwordx4 v[150:153], v2, s[8:9] offset:336
	global_load_dwordx4 v[146:149], v2, s[8:9] offset:320
	global_load_dwordx4 v[158:161], v2, s[8:9] offset:400
	global_load_dwordx4 v[154:157], v2, s[8:9] offset:384
	global_load_dwordx4 v[192:195], v2, s[8:9] offset:464
	global_load_dwordx4 v[178:181], v2, s[8:9] offset:448
	s_waitcnt lgkmcnt(3)
	v_lshlrev_b32_e32 v19, 16, v174
	s_waitcnt lgkmcnt(2)
	v_lshlrev_b32_e32 v28, 16, v170
	v_lshl_add_u64 v[16:17], s[8:9], 0, v[2:3]
	s_cmp_lg_u32 s76, 4
	s_cselect_b64 s[14:15], -1, 0
	s_cmp_eq_u32 s76, 4
	s_waitcnt vmcnt(14)
	v_fma_f32 v19, v19, v106, 0
	v_and_b32_e32 v24, 0xffff0000, v174
	v_fmac_f32_e32 v19, v24, v107
	v_lshlrev_b32_e32 v24, 16, v175
	v_fmac_f32_e32 v19, v24, v108
	v_and_b32_e32 v24, 0xffff0000, v175
	v_fmac_f32_e32 v19, v24, v109
	v_lshlrev_b32_e32 v24, 16, v176
	v_fmac_f32_e32 v19, v24, v110
	v_and_b32_e32 v20, 0xffff0000, v176
	v_fmac_f32_e32 v19, v20, v111
	v_lshlrev_b32_e32 v20, 16, v177
	v_fmac_f32_e32 v19, v20, v112
	v_and_b32_e32 v20, 0xffff0000, v177
	v_fmac_f32_e32 v19, v20, v113
	s_waitcnt vmcnt(12)
	v_fmac_f32_e32 v19, v28, v114
	v_and_b32_e32 v24, 0xffff0000, v170
	v_fmac_f32_e32 v19, v24, v115
	v_lshlrev_b32_e32 v24, 16, v171
	v_fmac_f32_e32 v19, v24, v116
	v_and_b32_e32 v24, 0xffff0000, v171
	v_fmac_f32_e32 v19, v24, v117
	v_lshlrev_b32_e32 v24, 16, v172
	v_fmac_f32_e32 v19, v24, v118
	v_and_b32_e32 v20, 0xffff0000, v172
	v_fmac_f32_e32 v19, v20, v119
	v_lshlrev_b32_e32 v20, 16, v173
	v_fmac_f32_e32 v19, v20, v120
	v_and_b32_e32 v20, 0xffff0000, v173
	v_fmac_f32_e32 v19, v20, v121
	s_waitcnt lgkmcnt(1)
	v_lshlrev_b32_e32 v28, 16, v166
	s_waitcnt vmcnt(10)
	v_fmac_f32_e32 v19, v28, v122
	v_and_b32_e32 v24, 0xffff0000, v166
	v_fmac_f32_e32 v19, v24, v123
	v_lshlrev_b32_e32 v24, 16, v167
	v_fmac_f32_e32 v19, v24, v124
	v_and_b32_e32 v24, 0xffff0000, v167
	v_fmac_f32_e32 v19, v24, v125
	v_lshlrev_b32_e32 v24, 16, v168
	v_fmac_f32_e32 v19, v24, v126
	v_and_b32_e32 v20, 0xffff0000, v168
	v_fmac_f32_e32 v19, v20, v127
	v_lshlrev_b32_e32 v20, 16, v169
	v_fmac_f32_e32 v19, v20, v128
	v_and_b32_e32 v20, 0xffff0000, v169
	v_fmac_f32_e32 v19, v20, v129
	ds_read_b128 v[28:31], v191 offset:3072
	s_waitcnt lgkmcnt(0)
	v_lshlrev_b32_e32 v34, 16, v28
	v_and_b32_e32 v35, 0xffff0000, v28
	v_lshlrev_b32_e32 v36, 16, v29
	v_and_b32_e32 v37, 0xffff0000, v29
	v_lshlrev_b32_e32 v38, 16, v30
	v_and_b32_e32 v39, 0xffff0000, v30
	v_lshlrev_b32_e32 v40, 16, v31
	v_and_b32_e32 v41, 0xffff0000, v31
	s_waitcnt vmcnt(8)
	v_fmac_f32_e32 v19, v34, v130
	v_fmac_f32_e32 v19, v35, v131
	v_fmac_f32_e32 v19, v36, v132
	v_fmac_f32_e32 v19, v37, v133
	v_fmac_f32_e32 v19, v38, v134
	v_fmac_f32_e32 v19, v39, v135
	v_fmac_f32_e32 v19, v40, v136
	v_fmac_f32_e32 v19, v41, v137
	ds_read_b128 v[28:31], v191 offset:4096
	s_waitcnt lgkmcnt(0)
	v_lshlrev_b32_e32 v42, 16, v28
	v_and_b32_e32 v43, 0xffff0000, v28
	v_lshlrev_b32_e32 v44, 16, v29
	v_and_b32_e32 v45, 0xffff0000, v29
	v_lshlrev_b32_e32 v46, 16, v30
	v_and_b32_e32 v47, 0xffff0000, v30
	v_lshlrev_b32_e32 v48, 16, v31
	v_and_b32_e32 v49, 0xffff0000, v31
	s_waitcnt vmcnt(6)
	v_fmac_f32_e32 v19, v42, v138
	v_fmac_f32_e32 v19, v43, v139
	v_fmac_f32_e32 v19, v44, v140
	v_fmac_f32_e32 v19, v45, v141
	v_fmac_f32_e32 v19, v46, v142
	v_fmac_f32_e32 v19, v47, v143
	v_fmac_f32_e32 v19, v48, v144
	v_fmac_f32_e32 v19, v49, v145
	ds_read_b128 v[28:31], v191 offset:5120
	s_waitcnt lgkmcnt(0)
	v_lshlrev_b32_e32 v50, 16, v28
	v_and_b32_e32 v51, 0xffff0000, v28
	v_lshlrev_b32_e32 v56, 16, v29
	v_and_b32_e32 v57, 0xffff0000, v29
	v_lshlrev_b32_e32 v58, 16, v30
	v_and_b32_e32 v59, 0xffff0000, v30
	v_lshlrev_b32_e32 v60, 16, v31
	v_and_b32_e32 v61, 0xffff0000, v31
	s_waitcnt vmcnt(4)
	v_fmac_f32_e32 v19, v50, v146
	v_fmac_f32_e32 v19, v51, v147
	v_fmac_f32_e32 v19, v56, v148
	v_fmac_f32_e32 v19, v57, v149
	v_fmac_f32_e32 v19, v58, v150
	v_fmac_f32_e32 v19, v59, v151
	v_fmac_f32_e32 v19, v60, v152
	v_fmac_f32_e32 v19, v61, v153
	ds_read_b128 v[28:31], v191 offset:6144
	s_waitcnt lgkmcnt(0)
	v_lshlrev_b32_e32 v62, 16, v28
	v_and_b32_e32 v63, 0xffff0000, v28
	v_lshlrev_b32_e32 v64, 16, v29
	v_and_b32_e32 v65, 0xffff0000, v29
	v_lshlrev_b32_e32 v66, 16, v30
	v_and_b32_e32 v67, 0xffff0000, v30
	v_lshlrev_b32_e32 v68, 16, v31
	v_and_b32_e32 v69, 0xffff0000, v31
	s_waitcnt vmcnt(2)
	v_fmac_f32_e32 v19, v62, v154
	v_fmac_f32_e32 v19, v63, v155
	v_fmac_f32_e32 v19, v64, v156
	v_fmac_f32_e32 v19, v65, v157
	v_fmac_f32_e32 v19, v66, v158
	v_fmac_f32_e32 v19, v67, v159
	v_fmac_f32_e32 v19, v68, v160
	v_fmac_f32_e32 v19, v69, v161
	ds_read_b128 v[30:33], v191 offset:7168
	s_waitcnt lgkmcnt(0)
	v_lshlrev_b32_e32 v25, 16, v30
	s_waitcnt vmcnt(0)
	v_fmac_f32_e32 v19, v25, v178
	v_and_b32_e32 v26, 0xffff0000, v30
	v_fmac_f32_e32 v19, v26, v179
	v_lshlrev_b32_e32 v27, 16, v31
	v_fmac_f32_e32 v19, v27, v180
	v_and_b32_e32 v28, 0xffff0000, v31
	v_fmac_f32_e32 v19, v28, v181
	v_lshlrev_b32_e32 v29, 16, v32
	v_fmac_f32_e32 v19, v29, v192
	v_and_b32_e32 v30, 0xffff0000, v32
	v_fmac_f32_e32 v19, v30, v193
	v_lshlrev_b32_e32 v31, 16, v33
	v_fmac_f32_e32 v19, v31, v194
	v_and_b32_e32 v32, 0xffff0000, v33
	v_fmac_f32_e32 v19, v32, v195
	global_load_dwordx4 v[110:113], v2, s[8:9] offset:528
	global_load_dwordx4 v[106:109], v2, s[8:9] offset:512
	global_load_dwordx4 v[118:121], v2, s[8:9] offset:592
	global_load_dwordx4 v[114:117], v2, s[8:9] offset:576
	global_load_dwordx4 v[126:129], v2, s[8:9] offset:656
	global_load_dwordx4 v[122:125], v2, s[8:9] offset:640
	global_load_dwordx4 v[134:137], v2, s[8:9] offset:720
	global_load_dwordx4 v[130:133], v2, s[8:9] offset:704
	global_load_dwordx4 v[142:145], v2, s[8:9] offset:784
	global_load_dwordx4 v[138:141], v2, s[8:9] offset:768
	global_load_dwordx4 v[150:153], v2, s[8:9] offset:848
	global_load_dwordx4 v[146:149], v2, s[8:9] offset:832
	global_load_dwordx4 v[158:161], v2, s[8:9] offset:912
	global_load_dwordx4 v[154:157], v2, s[8:9] offset:896
	global_load_dwordx4 v[192:195], v2, s[8:9] offset:976
	global_load_dwordx4 v[178:181], v2, s[8:9] offset:960
	ds_read_b128 v[74:77], v191
	v_mov_b32_e32 v24, v19
	s_nop 1
	v_permlane32_swap_b32_e32 v19, v24
	s_waitcnt lgkmcnt(0)
	v_lshlrev_b32_e32 v78, 16, v74
	v_and_b32_e32 v79, 0xffff0000, v74
	v_lshlrev_b32_e32 v80, 16, v75
	v_and_b32_e32 v81, 0xffff0000, v75
	v_lshlrev_b32_e32 v82, 16, v76
	v_and_b32_e32 v83, 0xffff0000, v76
	v_lshlrev_b32_e32 v84, 16, v77
	v_and_b32_e32 v85, 0xffff0000, v77
	s_waitcnt vmcnt(14)
	v_fma_f32 v33, v78, v106, 0
	v_fmac_f32_e32 v33, v79, v107
	v_fmac_f32_e32 v33, v80, v108
	v_fmac_f32_e32 v33, v81, v109
	v_fmac_f32_e32 v33, v82, v110
	v_fmac_f32_e32 v33, v83, v111
	v_fmac_f32_e32 v33, v84, v112
	v_fmac_f32_e32 v33, v85, v113
	ds_read_b128 v[86:89], v191 offset:1024
	s_waitcnt lgkmcnt(0)
	v_lshlrev_b32_e32 v70, 16, v86
	v_and_b32_e32 v71, 0xffff0000, v86
	v_lshlrev_b32_e32 v76, 16, v89
	v_and_b32_e32 v77, 0xffff0000, v89
	s_waitcnt vmcnt(12)
	v_fmac_f32_e32 v33, v70, v114
	v_fmac_f32_e32 v33, v71, v115
	v_lshlrev_b32_e32 v72, 16, v87
	v_fmac_f32_e32 v33, v72, v116
	v_and_b32_e32 v73, 0xffff0000, v87
	v_fmac_f32_e32 v33, v73, v117
	v_lshlrev_b32_e32 v74, 16, v88
	v_fmac_f32_e32 v33, v74, v118
	v_and_b32_e32 v75, 0xffff0000, v88
	v_fmac_f32_e32 v33, v75, v119
	v_fmac_f32_e32 v33, v76, v120
	v_fmac_f32_e32 v33, v77, v121
	ds_read_b128 v[92:95], v191 offset:2048
	s_waitcnt lgkmcnt(0)
	v_lshlrev_b32_e32 v86, 16, v92
	v_and_b32_e32 v87, 0xffff0000, v92
	v_lshlrev_b32_e32 v92, 16, v95
	s_waitcnt vmcnt(10)
	v_fmac_f32_e32 v33, v86, v122
	v_fmac_f32_e32 v33, v87, v123
	v_lshlrev_b32_e32 v88, 16, v93
	v_fmac_f32_e32 v33, v88, v124
	v_and_b32_e32 v89, 0xffff0000, v93
	v_fmac_f32_e32 v33, v89, v125
	v_lshlrev_b32_e32 v90, 16, v94
	v_fmac_f32_e32 v33, v90, v126
	v_and_b32_e32 v91, 0xffff0000, v94
	v_fmac_f32_e32 v33, v91, v127
	v_fmac_f32_e32 v33, v92, v128
	v_and_b32_e32 v93, 0xffff0000, v95
	v_fmac_f32_e32 v33, v93, v129
	s_waitcnt vmcnt(8)
	v_fmac_f32_e32 v33, v34, v130
	v_fmac_f32_e32 v33, v35, v131
	v_fmac_f32_e32 v33, v36, v132
	v_fmac_f32_e32 v33, v37, v133
	v_fmac_f32_e32 v33, v38, v134
	v_fmac_f32_e32 v33, v39, v135
	v_fmac_f32_e32 v33, v40, v136
	v_fmac_f32_e32 v33, v41, v137
	s_waitcnt vmcnt(6)
	v_fmac_f32_e32 v33, v42, v138
	v_fmac_f32_e32 v33, v43, v139
	v_fmac_f32_e32 v33, v44, v140
	v_fmac_f32_e32 v33, v45, v141
	v_fmac_f32_e32 v33, v46, v142
	v_fmac_f32_e32 v33, v47, v143
	v_fmac_f32_e32 v33, v48, v144
	v_fmac_f32_e32 v33, v49, v145
	s_waitcnt vmcnt(4)
	v_fmac_f32_e32 v33, v50, v146
	v_fmac_f32_e32 v33, v51, v147
	v_fmac_f32_e32 v33, v56, v148
	v_fmac_f32_e32 v33, v57, v149
	v_fmac_f32_e32 v33, v58, v150
	v_fmac_f32_e32 v33, v59, v151
	v_fmac_f32_e32 v33, v60, v152
	v_fmac_f32_e32 v33, v61, v153
	s_waitcnt vmcnt(2)
	v_fmac_f32_e32 v33, v62, v154
	v_fmac_f32_e32 v33, v63, v155
	v_fmac_f32_e32 v33, v64, v156
	v_fmac_f32_e32 v33, v65, v157
	v_fmac_f32_e32 v33, v66, v158
	v_fmac_f32_e32 v33, v67, v159
	v_fmac_f32_e32 v33, v68, v160
	v_fmac_f32_e32 v33, v69, v161
	s_waitcnt vmcnt(0)
	v_fmac_f32_e32 v33, v25, v178
	v_fmac_f32_e32 v33, v26, v179
	v_fmac_f32_e32 v33, v27, v180
	v_fmac_f32_e32 v33, v28, v181
	v_fmac_f32_e32 v33, v29, v192
	v_fmac_f32_e32 v33, v30, v193
	v_fmac_f32_e32 v33, v31, v194
	v_fmac_f32_e32 v33, v32, v195
	global_load_dwordx4 v[110:113], v2, s[8:9] offset:1040
	global_load_dwordx4 v[106:109], v2, s[8:9] offset:1024
	global_load_dwordx4 v[118:121], v2, s[8:9] offset:1104
	global_load_dwordx4 v[114:117], v2, s[8:9] offset:1088
	global_load_dwordx4 v[126:129], v2, s[8:9] offset:1168
	global_load_dwordx4 v[122:125], v2, s[8:9] offset:1152
	global_load_dwordx4 v[134:137], v2, s[8:9] offset:1232
	global_load_dwordx4 v[130:133], v2, s[8:9] offset:1216
	global_load_dwordx4 v[142:145], v2, s[8:9] offset:1296
	global_load_dwordx4 v[138:141], v2, s[8:9] offset:1280
	global_load_dwordx4 v[150:153], v2, s[8:9] offset:1360
	global_load_dwordx4 v[146:149], v2, s[8:9] offset:1344
	global_load_dwordx4 v[158:161], v2, s[8:9] offset:1424
	global_load_dwordx4 v[154:157], v2, s[8:9] offset:1408
	global_load_dwordx4 v[192:195], v2, s[8:9] offset:1488
	global_load_dwordx4 v[178:181], v2, s[8:9] offset:1472
	v_mov_b32_e32 v94, v33
	s_nop 1
	v_permlane32_swap_b32_e32 v33, v94
	s_waitcnt vmcnt(14)
	v_fma_f32 v95, v78, v106, 0
	v_fmac_f32_e32 v95, v79, v107
	v_fmac_f32_e32 v95, v80, v108
	v_fmac_f32_e32 v95, v81, v109
	v_fmac_f32_e32 v95, v82, v110
	v_fmac_f32_e32 v95, v83, v111
	v_fmac_f32_e32 v95, v84, v112
	v_fmac_f32_e32 v95, v85, v113
	s_waitcnt vmcnt(12)
	v_fmac_f32_e32 v95, v70, v114
	v_fmac_f32_e32 v95, v71, v115
	v_fmac_f32_e32 v95, v72, v116
	v_fmac_f32_e32 v95, v73, v117
	v_fmac_f32_e32 v95, v74, v118
	v_fmac_f32_e32 v95, v75, v119
	v_fmac_f32_e32 v95, v76, v120
	v_fmac_f32_e32 v95, v77, v121
	s_waitcnt vmcnt(10)
	v_fmac_f32_e32 v95, v86, v122
	v_fmac_f32_e32 v95, v87, v123
	v_fmac_f32_e32 v95, v88, v124
	v_fmac_f32_e32 v95, v89, v125
	v_fmac_f32_e32 v95, v90, v126
	v_fmac_f32_e32 v95, v91, v127
	v_fmac_f32_e32 v95, v92, v128
	v_fmac_f32_e32 v95, v93, v129
	s_waitcnt vmcnt(8)
	v_fmac_f32_e32 v95, v34, v130
	v_fmac_f32_e32 v95, v35, v131
	v_fmac_f32_e32 v95, v36, v132
	v_fmac_f32_e32 v95, v37, v133
	v_fmac_f32_e32 v95, v38, v134
	v_fmac_f32_e32 v95, v39, v135
	v_fmac_f32_e32 v95, v40, v136
	v_fmac_f32_e32 v95, v41, v137
	s_waitcnt vmcnt(6)
	v_fmac_f32_e32 v95, v42, v138
	v_fmac_f32_e32 v95, v43, v139
	v_fmac_f32_e32 v95, v44, v140
	v_fmac_f32_e32 v95, v45, v141
	v_fmac_f32_e32 v95, v46, v142
	v_fmac_f32_e32 v95, v47, v143
	v_fmac_f32_e32 v95, v48, v144
	v_fmac_f32_e32 v95, v49, v145
	s_waitcnt vmcnt(4)
	v_fmac_f32_e32 v95, v50, v146
	v_fmac_f32_e32 v95, v51, v147
	v_fmac_f32_e32 v95, v56, v148
	v_fmac_f32_e32 v95, v57, v149
	v_fmac_f32_e32 v95, v58, v150
	v_fmac_f32_e32 v95, v59, v151
	v_fmac_f32_e32 v95, v60, v152
	v_fmac_f32_e32 v95, v61, v153
	s_waitcnt vmcnt(2)
	v_fmac_f32_e32 v95, v62, v154
	v_fmac_f32_e32 v95, v63, v155
	v_fmac_f32_e32 v95, v64, v156
	v_fmac_f32_e32 v95, v65, v157
	v_fmac_f32_e32 v95, v66, v158
	v_fmac_f32_e32 v95, v67, v159
	v_fmac_f32_e32 v95, v68, v160
	v_fmac_f32_e32 v95, v69, v161
	s_waitcnt vmcnt(0)
	v_fmac_f32_e32 v95, v25, v178
	v_fmac_f32_e32 v95, v26, v179
	v_fmac_f32_e32 v95, v27, v180
	v_fmac_f32_e32 v95, v28, v181
	v_fmac_f32_e32 v95, v29, v192
	v_fmac_f32_e32 v95, v30, v193
	v_fmac_f32_e32 v95, v31, v194
	v_fmac_f32_e32 v95, v32, v195
	global_load_dwordx4 v[110:113], v2, s[8:9] offset:1552
	global_load_dwordx4 v[106:109], v2, s[8:9] offset:1536
	global_load_dwordx4 v[118:121], v2, s[8:9] offset:1616
	global_load_dwordx4 v[114:117], v2, s[8:9] offset:1600
	global_load_dwordx4 v[126:129], v2, s[8:9] offset:1680
	global_load_dwordx4 v[122:125], v2, s[8:9] offset:1664
	global_load_dwordx4 v[134:137], v2, s[8:9] offset:1744
	global_load_dwordx4 v[130:133], v2, s[8:9] offset:1728
	global_load_dwordx4 v[142:145], v2, s[8:9] offset:1808
	global_load_dwordx4 v[138:141], v2, s[8:9] offset:1792
	global_load_dwordx4 v[150:153], v2, s[8:9] offset:1872
	global_load_dwordx4 v[146:149], v2, s[8:9] offset:1856
	global_load_dwordx4 v[158:161], v2, s[8:9] offset:1936
	global_load_dwordx4 v[154:157], v2, s[8:9] offset:1920
	global_load_dwordx4 v[192:195], v2, s[8:9] offset:2000
	global_load_dwordx4 v[178:181], v2, s[8:9] offset:1984
	v_mov_b32_e32 v96, v95
	s_nop 1
	v_permlane32_swap_b32_e32 v95, v96
	s_waitcnt vmcnt(14)
	v_fma_f32 v97, v78, v106, 0
	v_fmac_f32_e32 v97, v79, v107
	v_fmac_f32_e32 v97, v80, v108
	v_fmac_f32_e32 v97, v81, v109
	v_fmac_f32_e32 v97, v82, v110
	v_fmac_f32_e32 v97, v83, v111
	v_fmac_f32_e32 v97, v84, v112
	v_fmac_f32_e32 v97, v85, v113
	s_waitcnt vmcnt(12)
	v_fmac_f32_e32 v97, v70, v114
	v_fmac_f32_e32 v97, v71, v115
	v_fmac_f32_e32 v97, v72, v116
	v_fmac_f32_e32 v97, v73, v117
	v_fmac_f32_e32 v97, v74, v118
	v_fmac_f32_e32 v97, v75, v119
	v_fmac_f32_e32 v97, v76, v120
	v_fmac_f32_e32 v97, v77, v121
	s_waitcnt vmcnt(10)
	v_fmac_f32_e32 v97, v86, v122
	v_fmac_f32_e32 v97, v87, v123
	v_fmac_f32_e32 v97, v88, v124
	v_fmac_f32_e32 v97, v89, v125
	v_fmac_f32_e32 v97, v90, v126
	v_fmac_f32_e32 v97, v91, v127
	v_fmac_f32_e32 v97, v92, v128
	v_fmac_f32_e32 v97, v93, v129
	s_waitcnt vmcnt(8)
	v_fmac_f32_e32 v97, v34, v130
	v_fmac_f32_e32 v97, v35, v131
	v_fmac_f32_e32 v97, v36, v132
	v_fmac_f32_e32 v97, v37, v133
	v_fmac_f32_e32 v97, v38, v134
	v_fmac_f32_e32 v97, v39, v135
	v_fmac_f32_e32 v97, v40, v136
	v_fmac_f32_e32 v97, v41, v137
	s_waitcnt vmcnt(6)
	v_fmac_f32_e32 v97, v42, v138
	v_fmac_f32_e32 v97, v43, v139
	v_fmac_f32_e32 v97, v44, v140
	v_fmac_f32_e32 v97, v45, v141
	v_fmac_f32_e32 v97, v46, v142
	v_fmac_f32_e32 v97, v47, v143
	v_fmac_f32_e32 v97, v48, v144
	v_fmac_f32_e32 v97, v49, v145
	s_waitcnt vmcnt(4)
	v_fmac_f32_e32 v97, v50, v146
	v_fmac_f32_e32 v97, v51, v147
	v_fmac_f32_e32 v97, v56, v148
	v_fmac_f32_e32 v97, v57, v149
	v_fmac_f32_e32 v97, v58, v150
	v_fmac_f32_e32 v97, v59, v151
	v_fmac_f32_e32 v97, v60, v152
	v_fmac_f32_e32 v97, v61, v153
	s_waitcnt vmcnt(2)
	v_fmac_f32_e32 v97, v62, v154
	v_fmac_f32_e32 v97, v63, v155
	v_fmac_f32_e32 v97, v64, v156
	v_fmac_f32_e32 v97, v65, v157
	v_fmac_f32_e32 v97, v66, v158
	v_fmac_f32_e32 v97, v67, v159
	v_fmac_f32_e32 v97, v68, v160
	v_fmac_f32_e32 v97, v69, v161
	s_waitcnt vmcnt(0)
	v_fmac_f32_e32 v97, v25, v178
	v_fmac_f32_e32 v97, v26, v179
	v_fmac_f32_e32 v97, v27, v180
	v_fmac_f32_e32 v97, v28, v181
	v_fmac_f32_e32 v97, v29, v192
	v_fmac_f32_e32 v97, v30, v193
	v_fmac_f32_e32 v97, v31, v194
	v_fmac_f32_e32 v97, v32, v195
	v_mov_b32_e32 v2, v97
	s_nop 1
	v_permlane32_swap_b32_e32 v97, v2
	v_mov_b32_e32 v21, 0xff800000
	v_mov_b32_e32 v20, 0xff800000
	s_cbranch_scc1 .LBB0_2649
	global_load_dwordx4 v[110:113], v[16:17], off offset:2064
	global_load_dwordx4 v[106:109], v[16:17], off offset:2048
	global_load_dwordx4 v[118:121], v[16:17], off offset:2128
	global_load_dwordx4 v[114:117], v[16:17], off offset:2112
	global_load_dwordx4 v[126:129], v[16:17], off offset:2192
	global_load_dwordx4 v[122:125], v[16:17], off offset:2176
	global_load_dwordx4 v[134:137], v[16:17], off offset:2256
	global_load_dwordx4 v[130:133], v[16:17], off offset:2240
	global_load_dwordx4 v[142:145], v[16:17], off offset:2320
	global_load_dwordx4 v[138:141], v[16:17], off offset:2304
	global_load_dwordx4 v[150:153], v[16:17], off offset:2384
	global_load_dwordx4 v[146:149], v[16:17], off offset:2368
	global_load_dwordx4 v[158:161], v[16:17], off offset:2448
	global_load_dwordx4 v[154:157], v[16:17], off offset:2432
	global_load_dwordx4 v[192:195], v[16:17], off offset:2512
	global_load_dwordx4 v[178:181], v[16:17], off offset:2496
	s_waitcnt vmcnt(14)
	v_fma_f32 v20, v78, v106, 0
	v_fmac_f32_e32 v20, v79, v107
	v_fmac_f32_e32 v20, v80, v108
	v_fmac_f32_e32 v20, v81, v109
	v_fmac_f32_e32 v20, v82, v110
	v_fmac_f32_e32 v20, v83, v111
	v_fmac_f32_e32 v20, v84, v112
	v_fmac_f32_e32 v20, v85, v113
	s_waitcnt vmcnt(12)
	v_fmac_f32_e32 v20, v70, v114
	v_fmac_f32_e32 v20, v71, v115
	v_fmac_f32_e32 v20, v72, v116
	v_fmac_f32_e32 v20, v73, v117
	v_fmac_f32_e32 v20, v74, v118
	v_fmac_f32_e32 v20, v75, v119
	v_fmac_f32_e32 v20, v76, v120
	v_fmac_f32_e32 v20, v77, v121
	s_waitcnt vmcnt(10)
	v_fmac_f32_e32 v20, v86, v122
	v_fmac_f32_e32 v20, v87, v123
	v_fmac_f32_e32 v20, v88, v124
	v_fmac_f32_e32 v20, v89, v125
	v_fmac_f32_e32 v20, v90, v126
	v_fmac_f32_e32 v20, v91, v127
	v_fmac_f32_e32 v20, v92, v128
	v_fmac_f32_e32 v20, v93, v129
	s_waitcnt vmcnt(8)
	v_fmac_f32_e32 v20, v34, v130
	v_fmac_f32_e32 v20, v35, v131
	v_fmac_f32_e32 v20, v36, v132
	v_fmac_f32_e32 v20, v37, v133
	v_fmac_f32_e32 v20, v38, v134
	v_fmac_f32_e32 v20, v39, v135
	v_fmac_f32_e32 v20, v40, v136
	v_fmac_f32_e32 v20, v41, v137
	s_waitcnt vmcnt(6)
	v_fmac_f32_e32 v20, v42, v138
	v_fmac_f32_e32 v20, v43, v139
	v_fmac_f32_e32 v20, v44, v140
	v_fmac_f32_e32 v20, v45, v141
	v_fmac_f32_e32 v20, v46, v142
	v_fmac_f32_e32 v20, v47, v143
	v_fmac_f32_e32 v20, v48, v144
	v_fmac_f32_e32 v20, v49, v145
	s_waitcnt vmcnt(4)
	v_fmac_f32_e32 v20, v50, v146
	v_fmac_f32_e32 v20, v51, v147
	v_fmac_f32_e32 v20, v56, v148
	v_fmac_f32_e32 v20, v57, v149
	v_fmac_f32_e32 v20, v58, v150
	v_fmac_f32_e32 v20, v59, v151
	v_fmac_f32_e32 v20, v60, v152
	v_fmac_f32_e32 v20, v61, v153
	s_waitcnt vmcnt(2)
	v_fmac_f32_e32 v20, v62, v154
	v_fmac_f32_e32 v20, v63, v155
	v_fmac_f32_e32 v20, v64, v156
	v_fmac_f32_e32 v20, v65, v157
	v_fmac_f32_e32 v20, v66, v158
	v_fmac_f32_e32 v20, v67, v159
	v_fmac_f32_e32 v20, v68, v160
	v_fmac_f32_e32 v20, v69, v161
	s_waitcnt vmcnt(0)
	v_fmac_f32_e32 v20, v25, v178
	v_fmac_f32_e32 v20, v26, v179
	v_fmac_f32_e32 v20, v27, v180
	v_fmac_f32_e32 v20, v28, v181
	v_fmac_f32_e32 v20, v29, v192
	v_fmac_f32_e32 v20, v30, v193
	v_fmac_f32_e32 v20, v31, v194
	v_fmac_f32_e32 v20, v32, v195
	v_mov_b32_e32 v22, v20
	s_nop 1
	v_permlane32_swap_b32_e32 v20, v22
	v_add_f32_e32 v20, v20, v22
.LBB0_2649:
	s_cmpk_gt_u32 s24, 0x5ff
	s_cselect_b64 s[12:13], -1, 0
	s_cmpk_lt_u32 s24, 0x600
	s_cbranch_scc1 .LBB0_2651
	global_load_dwordx4 v[110:113], v[16:17], off offset:2576
	global_load_dwordx4 v[106:109], v[16:17], off offset:2560
	global_load_dwordx4 v[118:121], v[16:17], off offset:2640
	global_load_dwordx4 v[114:117], v[16:17], off offset:2624
	global_load_dwordx4 v[126:129], v[16:17], off offset:2704
	global_load_dwordx4 v[122:125], v[16:17], off offset:2688
	global_load_dwordx4 v[134:137], v[16:17], off offset:2768
	global_load_dwordx4 v[130:133], v[16:17], off offset:2752
	global_load_dwordx4 v[142:145], v[16:17], off offset:2832
	global_load_dwordx4 v[138:141], v[16:17], off offset:2816
	global_load_dwordx4 v[150:153], v[16:17], off offset:2896
	global_load_dwordx4 v[146:149], v[16:17], off offset:2880
	global_load_dwordx4 v[158:161], v[16:17], off offset:2960
	global_load_dwordx4 v[154:157], v[16:17], off offset:2944
	global_load_dwordx4 v[192:195], v[16:17], off offset:3024
	global_load_dwordx4 v[178:181], v[16:17], off offset:3008
	s_waitcnt vmcnt(14)
	v_fma_f32 v21, v78, v106, 0
	v_fmac_f32_e32 v21, v79, v107
	v_fmac_f32_e32 v21, v80, v108
	v_fmac_f32_e32 v21, v81, v109
	v_fmac_f32_e32 v21, v82, v110
	v_fmac_f32_e32 v21, v83, v111
	v_fmac_f32_e32 v21, v84, v112
	v_fmac_f32_e32 v21, v85, v113
	s_waitcnt vmcnt(12)
	v_fmac_f32_e32 v21, v70, v114
	v_fmac_f32_e32 v21, v71, v115
	v_fmac_f32_e32 v21, v72, v116
	v_fmac_f32_e32 v21, v73, v117
	v_fmac_f32_e32 v21, v74, v118
	v_fmac_f32_e32 v21, v75, v119
	v_fmac_f32_e32 v21, v76, v120
	v_fmac_f32_e32 v21, v77, v121
	s_waitcnt vmcnt(10)
	v_fmac_f32_e32 v21, v86, v122
	v_fmac_f32_e32 v21, v87, v123
	v_fmac_f32_e32 v21, v88, v124
	v_fmac_f32_e32 v21, v89, v125
	v_fmac_f32_e32 v21, v90, v126
	v_fmac_f32_e32 v21, v91, v127
	v_fmac_f32_e32 v21, v92, v128
	v_fmac_f32_e32 v21, v93, v129
	s_waitcnt vmcnt(8)
	v_fmac_f32_e32 v21, v34, v130
	v_fmac_f32_e32 v21, v35, v131
	v_fmac_f32_e32 v21, v36, v132
	v_fmac_f32_e32 v21, v37, v133
	v_fmac_f32_e32 v21, v38, v134
	v_fmac_f32_e32 v21, v39, v135
	v_fmac_f32_e32 v21, v40, v136
	v_fmac_f32_e32 v21, v41, v137
	s_waitcnt vmcnt(6)
	v_fmac_f32_e32 v21, v42, v138
	v_fmac_f32_e32 v21, v43, v139
	v_fmac_f32_e32 v21, v44, v140
	v_fmac_f32_e32 v21, v45, v141
	v_fmac_f32_e32 v21, v46, v142
	v_fmac_f32_e32 v21, v47, v143
	v_fmac_f32_e32 v21, v48, v144
	v_fmac_f32_e32 v21, v49, v145
	s_waitcnt vmcnt(4)
	v_fmac_f32_e32 v21, v50, v146
	v_fmac_f32_e32 v21, v51, v147
	v_fmac_f32_e32 v21, v56, v148
	v_fmac_f32_e32 v21, v57, v149
	v_fmac_f32_e32 v21, v58, v150
	v_fmac_f32_e32 v21, v59, v151
	v_fmac_f32_e32 v21, v60, v152
	v_fmac_f32_e32 v21, v61, v153
	s_waitcnt vmcnt(2)
	v_fmac_f32_e32 v21, v62, v154
	v_fmac_f32_e32 v21, v63, v155
	v_fmac_f32_e32 v21, v64, v156
	v_fmac_f32_e32 v21, v65, v157
	v_fmac_f32_e32 v21, v66, v158
	v_fmac_f32_e32 v21, v67, v159
	v_fmac_f32_e32 v21, v68, v160
	v_fmac_f32_e32 v21, v69, v161
	s_waitcnt vmcnt(0)
	v_fmac_f32_e32 v21, v25, v178
	v_fmac_f32_e32 v21, v26, v179
	v_fmac_f32_e32 v21, v27, v180
	v_fmac_f32_e32 v21, v28, v181
	v_fmac_f32_e32 v21, v29, v192
	v_fmac_f32_e32 v21, v30, v193
	v_fmac_f32_e32 v21, v31, v194
	v_fmac_f32_e32 v21, v32, v195
	v_mov_b32_e32 v22, v21
	s_nop 1
	v_permlane32_swap_b32_e32 v21, v22
	v_add_f32_e32 v21, v21, v22
.LBB0_2651:
	s_cmpk_gt_u32 s24, 0x6ff
	s_cselect_b64 s[8:9], -1, 0
	s_cmpk_lt_u32 s24, 0x700
	v_mov_b32_e32 v22, 0xff800000
	s_cbranch_scc1 .LBB0_2653
	global_load_dwordx4 v[110:113], v[16:17], off offset:3088
	global_load_dwordx4 v[106:109], v[16:17], off offset:3072
	global_load_dwordx4 v[118:121], v[16:17], off offset:3152
	global_load_dwordx4 v[114:117], v[16:17], off offset:3136
	global_load_dwordx4 v[126:129], v[16:17], off offset:3216
	global_load_dwordx4 v[122:125], v[16:17], off offset:3200
	global_load_dwordx4 v[134:137], v[16:17], off offset:3280
	global_load_dwordx4 v[130:133], v[16:17], off offset:3264
	global_load_dwordx4 v[142:145], v[16:17], off offset:3344
	global_load_dwordx4 v[138:141], v[16:17], off offset:3328
	global_load_dwordx4 v[150:153], v[16:17], off offset:3408
	global_load_dwordx4 v[146:149], v[16:17], off offset:3392
	global_load_dwordx4 v[158:161], v[16:17], off offset:3472
	global_load_dwordx4 v[154:157], v[16:17], off offset:3456
	global_load_dwordx4 v[192:195], v[16:17], off offset:3536
	global_load_dwordx4 v[178:181], v[16:17], off offset:3520
	s_waitcnt vmcnt(14)
	v_fma_f32 v22, v78, v106, 0
	v_fmac_f32_e32 v22, v79, v107
	v_fmac_f32_e32 v22, v80, v108
	v_fmac_f32_e32 v22, v81, v109
	v_fmac_f32_e32 v22, v82, v110
	v_fmac_f32_e32 v22, v83, v111
	v_fmac_f32_e32 v22, v84, v112
	v_fmac_f32_e32 v22, v85, v113
	s_waitcnt vmcnt(12)
	v_fmac_f32_e32 v22, v70, v114
	v_fmac_f32_e32 v22, v71, v115
	v_fmac_f32_e32 v22, v72, v116
	v_fmac_f32_e32 v22, v73, v117
	v_fmac_f32_e32 v22, v74, v118
	v_fmac_f32_e32 v22, v75, v119
	v_fmac_f32_e32 v22, v76, v120
	v_fmac_f32_e32 v22, v77, v121
	s_waitcnt vmcnt(10)
	v_fmac_f32_e32 v22, v86, v122
	v_fmac_f32_e32 v22, v87, v123
	v_fmac_f32_e32 v22, v88, v124
	v_fmac_f32_e32 v22, v89, v125
	v_fmac_f32_e32 v22, v90, v126
	v_fmac_f32_e32 v22, v91, v127
	v_fmac_f32_e32 v22, v92, v128
	v_fmac_f32_e32 v22, v93, v129
	s_waitcnt vmcnt(8)
	v_fmac_f32_e32 v22, v34, v130
	v_fmac_f32_e32 v22, v35, v131
	v_fmac_f32_e32 v22, v36, v132
	v_fmac_f32_e32 v22, v37, v133
	v_fmac_f32_e32 v22, v38, v134
	v_fmac_f32_e32 v22, v39, v135
	v_fmac_f32_e32 v22, v40, v136
	v_fmac_f32_e32 v22, v41, v137
	s_waitcnt vmcnt(6)
	v_fmac_f32_e32 v22, v42, v138
	v_fmac_f32_e32 v22, v43, v139
	v_fmac_f32_e32 v22, v44, v140
	v_fmac_f32_e32 v22, v45, v141
	v_fmac_f32_e32 v22, v46, v142
	v_fmac_f32_e32 v22, v47, v143
	v_fmac_f32_e32 v22, v48, v144
	v_fmac_f32_e32 v22, v49, v145
	s_waitcnt vmcnt(4)
	v_fmac_f32_e32 v22, v50, v146
	v_fmac_f32_e32 v22, v51, v147
	v_fmac_f32_e32 v22, v56, v148
	v_fmac_f32_e32 v22, v57, v149
	v_fmac_f32_e32 v22, v58, v150
	v_fmac_f32_e32 v22, v59, v151
	v_fmac_f32_e32 v22, v60, v152
	v_fmac_f32_e32 v22, v61, v153
	s_waitcnt vmcnt(2)
	v_fmac_f32_e32 v22, v62, v154
	v_fmac_f32_e32 v22, v63, v155
	v_fmac_f32_e32 v22, v64, v156
	v_fmac_f32_e32 v22, v65, v157
	v_fmac_f32_e32 v22, v66, v158
	v_fmac_f32_e32 v22, v67, v159
	v_fmac_f32_e32 v22, v68, v160
	v_fmac_f32_e32 v22, v69, v161
	s_waitcnt vmcnt(0)
	v_fmac_f32_e32 v22, v25, v178
	v_fmac_f32_e32 v22, v26, v179
	v_fmac_f32_e32 v22, v27, v180
	v_fmac_f32_e32 v22, v28, v181
	v_fmac_f32_e32 v22, v29, v192
	v_fmac_f32_e32 v22, v30, v193
	v_fmac_f32_e32 v22, v31, v194
	v_fmac_f32_e32 v22, v32, v195
	v_mov_b32_e32 v16, v22
	s_nop 1
	v_permlane32_swap_b32_e32 v22, v16
	v_add_f32_e32 v22, v22, v16
